# norm1's residual-stream stores non-temporal (next read five phases later)
# baseline (speedup 1.0000x reference)
.LBB0_331:
	s_waitcnt vmcnt(3)
	v_pk_mul_f32 v[64:65], v[14:15], v[14:15]
	s_waitcnt vmcnt(2)
	v_pk_mul_f32 v[66:67], v[10:11], v[10:11]
	v_pk_mul_f32 v[58:59], v[16:17], v[16:17]
	v_pk_mul_f32 v[62:63], v[12:13], v[12:13]
	v_mov_b32_e32 v68, v64
	v_mov_b32_e32 v69, v66
	v_mov_b32_e32 v66, v65
	v_pk_add_f32 v[64:65], v[68:69], v[66:67]
	v_mov_b32_e32 v66, v58
	v_mov_b32_e32 v67, v62
	s_waitcnt vmcnt(0)
	v_pk_mul_f32 v[54:55], v[2:3], v[2:3]
	v_pk_mul_f32 v[56:57], v[6:7], v[6:7]
	v_pk_add_f32 v[64:65], v[66:67], v[64:65]
	v_mov_b32_e32 v62, v59
	v_pk_mul_f32 v[50:51], v[4:5], v[4:5]
	v_pk_mul_f32 v[52:53], v[8:9], v[8:9]
	v_pk_add_f32 v[58:59], v[62:63], v[64:65]
	v_mov_b32_e32 v62, v54
	v_mov_b32_e32 v63, v56
	v_mov_b32_e32 v56, v55
	v_pk_add_f32 v[54:55], v[62:63], v[56:57]
	v_mov_b32_e32 v56, v50
	v_mov_b32_e32 v57, v52
	v_pk_add_f32 v[54:55], v[56:57], v[54:55]
	v_mov_b32_e32 v52, v51
	v_pk_add_f32 v[50:51], v[52:53], v[54:55]
	v_add_f32_e32 v37, v58, v59
	v_add_f32_e32 v37, v51, v37
	v_add_f32_e32 v37, v50, v37
	v_lshlrev_b64 v[62:63], 10, v[40:41]
	v_lshlrev_b64 v[40:41], 11, v[40:41]
	v_add_f32_dpp v37, v37, v37 quad_perm:[1,0,3,2] row_mask:0xf bank_mask:0xf
	v_cvt_pk_bf16_f32 v52, v14, v15
	v_cvt_pk_bf16_f32 v53, v16, v17
	v_add_f32_dpp v37, v37, v37 quad_perm:[2,3,0,1] row_mask:0xf bank_mask:0xf
	v_lshl_add_u64 v[64:65], v[22:23], 0, v[40:41]
	global_store_dwordx2 v[64:65], v[52:53], off nt
	v_add_f32_dpp v37, v37, v37 row_half_mirror row_mask:0xf bank_mask:0xf
	ds_read_b128 v[52:55], v73 offset:8192
	ds_read_b128 v[56:59], v73 offset:12288
	v_add_f32_dpp v37, v37, v37 row_mirror row_mask:0xf bank_mask:0xf
	s_nop 1
	v_add_f32_dpp v37, v37, v37 row_bcast:15 row_mask:0xa bank_mask:0xf
	s_nop 1
	v_add_f32_dpp v37, v37, v37 row_bcast:31 row_mask:0xc bank_mask:0xf
	s_nop 0
	v_readlane_b32 s100, v37, 63
	s_nop 1
	v_mov_b32_e32 v37, s100
	s_waitcnt lgkmcnt(0)
	v_fmamk_f32 v37, v37, 0x3a800000, v176
	v_cmp_gt_f32_e32 vcc, s25, v37
	v_mul_f32_e32 v39, 0x4b800000, v37
	s_nop 0
	v_cndmask_b32_e32 v37, v37, v39, vcc
	v_rsq_f32_e32 v37, v37
	s_nop 0
	v_mul_f32_e32 v39, 0x45800000, v37
	v_cndmask_b32_e32 v50, v37, v39, vcc
	v_pk_mul_f32 v[14:15], v[14:15], v[50:51] op_sel_hi:[1,0]
	v_mov_b32_e32 v37, v131
	v_pk_fma_f32 v[14:15], v[52:53], v[14:15], v[56:57]
	v_pk_mul_f32 v[16:17], v[16:17], v[50:51] op_sel_hi:[1,0]
	v_cvt_pk_bf16_f32 v52, v14, v15
	v_med3_f32 v14, v14, s26, v209
	v_med3_f32 v15, v15, s26, v209
	v_cvt_pk_fp8_f32 v37, v14, v15
	v_pk_fma_f32 v[54:55], v[54:55], v[16:17], v[58:59]
	v_lshl_add_u64 v[16:17], v[30:31], 0, v[40:41]
	v_med3_f32 v14, v54, s26, v209
	v_med3_f32 v15, v55, s26, v209
	v_cvt_pk_fp8_f32 v37, v14, v15 op_sel:[0,0,1]
	v_cvt_pk_bf16_f32 v53, v54, v55
	v_lshl_add_u64 v[14:15], v[32:33], 0, v[62:63]
	v_cvt_pk_bf16_f32 v40, v10, v11
	v_cvt_pk_bf16_f32 v41, v12, v13
	global_store_dwordx2 v[16:17], v[52:53], off
	global_store_dword v[14:15], v37, off
	global_store_dwordx2 v[64:65], v[40:41], off offset:512 nt
	ds_read_b128 v[52:55], v73 offset:9216
	ds_read_b128 v[56:59], v73 offset:13312
	v_pk_mul_f32 v[10:11], v[10:11], v[50:51] op_sel_hi:[1,0]
	v_mov_b32_e32 v37, v131
	v_pk_mul_f32 v[12:13], v[12:13], v[50:51] op_sel_hi:[1,0]
	v_cmp_le_i32_e32 vcc, s2, v60
	s_waitcnt lgkmcnt(0)
	v_pk_fma_f32 v[10:11], v[52:53], v[10:11], v[56:57]
	v_pk_fma_f32 v[12:13], v[54:55], v[12:13], v[58:59]
	v_cvt_pk_bf16_f32 v40, v10, v11
	v_med3_f32 v10, v10, s26, v209
	v_med3_f32 v11, v11, s26, v209
	v_cvt_pk_fp8_f32 v37, v10, v11
	v_med3_f32 v10, v12, s26, v209
	v_med3_f32 v11, v13, s26, v209
	v_cvt_pk_bf16_f32 v41, v12, v13
	v_cvt_pk_fp8_f32 v37, v10, v11 op_sel:[0,0,1]
	v_cvt_pk_bf16_f32 v10, v6, v7
	v_cvt_pk_bf16_f32 v11, v8, v9
	global_store_dwordx2 v[16:17], v[40:41], off offset:512
	global_store_dword v[14:15], v37, off offset:256
	global_store_dwordx2 v[64:65], v[10:11], off offset:1024 nt
	ds_read_b128 v[10:13], v73 offset:10240
	ds_read_b128 v[52:55], v73 offset:14336
	v_pk_mul_f32 v[6:7], v[6:7], v[50:51] op_sel_hi:[1,0]
	v_pk_mul_f32 v[8:9], v[8:9], v[50:51] op_sel_hi:[1,0]
	s_or_b64 s[70:71], vcc, s[70:71]
	v_mov_b64_e32 v[56:57], v[48:49]
	s_waitcnt lgkmcnt(0)
	v_pk_fma_f32 v[8:9], v[8:9], v[12:13], v[54:55]
	v_pk_fma_f32 v[6:7], v[6:7], v[10:11], v[52:53]
	v_cvt_pk_bf16_f32 v11, v8, v9
	v_cvt_pk_bf16_f32 v10, v6, v7
	global_store_dwordx2 v[16:17], v[10:11], off offset:1024
	v_med3_f32 v6, v6, s26, v209
	v_med3_f32 v7, v7, s26, v209
	v_mov_b32_e32 v10, v131
	v_cvt_pk_fp8_f32 v10, v6, v7
	v_med3_f32 v6, v8, s26, v209
	v_med3_f32 v7, v9, s26, v209
	v_mov_b64_e32 v[52:53], v[44:45]
	v_cvt_pk_fp8_f32 v10, v6, v7 op_sel:[0,0,1]
	v_cvt_pk_bf16_f32 v6, v2, v3
	v_cvt_pk_bf16_f32 v7, v4, v5
	v_pk_mul_f32 v[2:3], v[2:3], v[50:51] op_sel_hi:[1,0]
	global_store_dword v[14:15], v10, off offset:512
	global_store_dwordx2 v[64:65], v[6:7], off offset:1536 nt
	ds_read_b128 v[6:9], v73 offset:11264
	ds_read_b128 v[10:13], v73 offset:15360
	v_pk_mul_f32 v[4:5], v[4:5], v[50:51] op_sel_hi:[1,0]
	v_mov_b64_e32 v[50:51], v[42:43]
	v_mov_b64_e32 v[54:55], v[46:47]
	v_mov_b32_e32 v37, v61
	s_waitcnt lgkmcnt(0)
	v_pk_fma_f32 v[4:5], v[4:5], v[8:9], v[12:13]
	v_pk_fma_f32 v[2:3], v[2:3], v[6:7], v[10:11]
	v_cvt_pk_bf16_f32 v7, v4, v5
	v_cvt_pk_bf16_f32 v6, v2, v3
	global_store_dwordx2 v[16:17], v[6:7], off offset:1536
	v_med3_f32 v2, v2, s26, v209
	v_med3_f32 v3, v3, s26, v209
	v_mov_b32_e32 v6, v131
	v_cvt_pk_fp8_f32 v6, v2, v3
	v_med3_f32 v2, v4, s26, v209
	v_med3_f32 v3, v5, s26, v209
	v_mov_b32_e32 v39, v72
	v_cvt_pk_fp8_f32 v6, v2, v3 op_sel:[0,0,1]
	v_mov_b32_e32 v40, v60
	global_store_dword v[14:15], v6, off offset:768
	s_andn2_b64 exec, exec, s[70:71]
	s_cbranch_execz .LBB0_306
